# speedup vs baseline: 1.0015x; 1.0015x over previous
.LBB0_2:
	s_or_b64 exec, exec, s[8:9]
	s_add_u32 s4, s4, s24
	s_addc_u32 s5, s5, s25
	s_movk_i32 s3, 0x2b7
	v_cmp_gt_u32_e64 s[8:9], s3, v0
	v_lshlrev_b32_e32 v35, 2, v0
	v_mov_b32_e32 v34, 0
	s_and_saveexec_b64 s[50:51], s[8:9]
	ds_write_b32 v35, v34 offset:50000
	s_or_b64 exec, exec, s[50:51]
	s_waitcnt lgkmcnt(0)
	s_barrier
	global_load_dwordx4 v[30:33], v44, s[4:5] nt
	global_load_dwordx4 v[22:25], v45, s[4:5] nt
	global_load_dwordx4 v[14:17], v47, s[4:5] nt
	s_and_saveexec_b64 s[6:7], vcc
	s_cbranch_execz .LBB0_4
	global_load_dwordx4 v[6:9], v46, s[4:5] nt
.LBB0_4:
	s_or_b64 exec, exec, s[6:7]
	s_movk_i32 s3, 0x2b7
	v_cmp_gt_u32_e64 s[6:7], s3, v0
	v_lshlrev_b32_e32 v1, 2, v0
	s_and_saveexec_b64 s[4:5], s[6:7]
	s_or_b64 exec, exec, s[4:5]
	s_mov_b32 s3, 0x38e38e39
	s_waitcnt vmcnt(5)
	v_mul_hi_u32 v34, v26, s3
	v_lshrrev_b32_e32 v87, 5, v34
	v_mul_hi_u32 v35, v27, s3
	v_lshlrev_b32_e32 v84, 2, v87
	v_mov_b32_e32 v34, 1
	v_lshrrev_b32_e32 v77, 5, v35
	v_mul_hi_u32 v35, v28, s3
	s_waitcnt lgkmcnt(0)
	ds_add_rtn_u32 v86, v84, v34 offset:50000
	v_lshlrev_b32_e32 v85, 2, v77
	v_lshrrev_b32_e32 v75, 5, v35
	v_mul_hi_u32 v35, v29, s3
	ds_add_rtn_u32 v76, v85, v34 offset:50000
	v_lshlrev_b32_e32 v83, 2, v75
	v_lshrrev_b32_e32 v73, 5, v35
	s_waitcnt vmcnt(4)
	v_mul_hi_u32 v35, v18, s3
	ds_add_rtn_u32 v74, v83, v34 offset:50000
	v_lshlrev_b32_e32 v82, 2, v73
	v_lshrrev_b32_e32 v71, 5, v35
	v_mul_hi_u32 v35, v19, s3
	ds_add_rtn_u32 v72, v82, v34 offset:50000
	v_lshlrev_b32_e32 v81, 2, v71
	v_lshrrev_b32_e32 v69, 5, v35
	v_mul_hi_u32 v35, v20, s3
	ds_add_rtn_u32 v70, v81, v34 offset:50000
	v_lshlrev_b32_e32 v80, 2, v69
	v_lshrrev_b32_e32 v67, 5, v35
	v_mul_hi_u32 v35, v21, s3
	ds_add_rtn_u32 v68, v80, v34 offset:50000
	v_lshlrev_b32_e32 v79, 2, v67
	v_lshrrev_b32_e32 v65, 5, v35
	s_waitcnt vmcnt(3)
	v_mul_hi_u32 v35, v10, s3
	ds_add_rtn_u32 v66, v79, v34 offset:50000
	v_lshlrev_b32_e32 v78, 2, v65
	v_lshrrev_b32_e32 v62, 5, v35
	v_mul_hi_u32 v35, v11, s3
	ds_add_rtn_u32 v63, v78, v34 offset:50000
	v_lshlrev_b32_e32 v64, 2, v62
	v_lshrrev_b32_e32 v57, 5, v35
	v_mul_hi_u32 v35, v12, s3
	ds_add_rtn_u32 v60, v64, v34 offset:50000
	v_lshlrev_b32_e32 v61, 2, v57
	v_lshrrev_b32_e32 v55, 5, v35
	v_mul_hi_u32 v35, v13, s3
	ds_add_rtn_u32 v56, v61, v34 offset:50000
	v_lshlrev_b32_e32 v59, 2, v55
	v_lshrrev_b32_e32 v53, 5, v35
	ds_add_rtn_u32 v54, v59, v34 offset:50000
	v_lshlrev_b32_e32 v58, 2, v53
	ds_add_rtn_u32 v52, v58, v34 offset:50000
	v_cmp_gt_u32_e64 s[4:5], 53, v0
	v_mov_b32_e32 v88, 0
	v_mov_b32_e32 v51, 0
	v_mov_b32_e32 v50, 0
	v_mov_b32_e32 v49, 0
	v_mov_b32_e32 v48, 0
	s_and_saveexec_b64 s[8:9], s[4:5]
	s_cbranch_execz .LBB0_8
	v_mul_hi_u32 v35, v2, s3
	v_lshrrev_b32_e32 v35, 3, v35
	v_and_b32_e32 v35, 0x7fffffc, v35
	ds_add_rtn_u32 v51, v35, v34 offset:50000
	v_mul_hi_u32 v35, v3, s3
	v_lshrrev_b32_e32 v35, 3, v35
	v_and_b32_e32 v35, 0x7fffffc, v35
	ds_add_rtn_u32 v50, v35, v34 offset:50000
	v_mul_hi_u32 v35, v4, s3
	v_lshrrev_b32_e32 v35, 3, v35
	v_and_b32_e32 v35, 0x7fffffc, v35
	ds_add_rtn_u32 v49, v35, v34 offset:50000
	v_mul_hi_u32 v35, v5, s3
	v_lshrrev_b32_e32 v35, 3, v35
	v_and_b32_e32 v35, 0x7fffffc, v35
	ds_add_rtn_u32 v48, v35, v34 offset:50000
